# MLA step loop control flow: single barrier sequence (vmcnt(4)) without selection branches, rescale blocks out of line, one back-edge branch
# baseline (speedup 1.0000x reference)
.LBB0_1146:
.LBB0_1147:
	s_waitcnt vmcnt(4) lgkmcnt(0)
	s_barrier

.LBB0_1153:
	v_mfma_f32_32x32x16_bf16 v[4:19], v[140:143], v[172:175], v[4:19]
	v_exp_f32_e32 v100, v100
	v_exp_f32_e32 v101, v101
	v_exp_f32_e32 v102, v102
	v_exp_f32_e32 v103, v103
	v_mfma_f32_32x32x16_bf16 v[20:35], v[140:143], v[68:71], v[20:35]
	v_exp_f32_e32 v104, v104
	v_exp_f32_e32 v105, v105
	v_exp_f32_e32 v106, v106
	v_exp_f32_e32 v107, v107
	s_and_b32 s12, s27, 3
	s_mulk_i32 s12, 0x3000
	v_add_u32_e32 v140, s12, v188
	v_lshl_add_u32 v141, s18, 13, v186
	v_mfma_f32_32x32x16_bf16 v[4:19], v[144:147], v[72:75], v[4:19]
	v_exp_f32_e32 v108, v108
	v_exp_f32_e32 v109, v109
	v_exp_f32_e32 v110, v110
	v_exp_f32_e32 v111, v111
	v_mfma_f32_32x32x16_bf16 v[20:35], v[144:147], v[76:79], v[20:35]
	v_exp_f32_e32 v112, v112
	v_exp_f32_e32 v113, v113
	v_exp_f32_e32 v114, v114
	v_exp_f32_e32 v115, v115
	v_mfma_f32_32x32x16_bf16 v[4:19], v[148:151], v[80:83], v[4:19]
	v_exp_f32_e32 v84, v84
	v_exp_f32_e32 v85, v85
	v_exp_f32_e32 v86, v86
	v_exp_f32_e32 v87, v87
	v_mfma_f32_32x32x16_bf16 v[20:35], v[148:151], v[52:55], v[20:35]
	v_exp_f32_e32 v88, v88
	v_exp_f32_e32 v89, v89
	v_exp_f32_e32 v90, v90
	v_exp_f32_e32 v91, v91
	v_mfma_f32_32x32x16_bf16 v[4:19], v[152:155], v[56:59], v[4:19]
	v_mfma_f32_32x32x16_bf16 v[20:35], v[152:155], v[60:63], v[20:35]
	s_and_b64 vcc, exec, s[10:11]
	s_cbranch_vccnz .Lmla_resc1
.LBB0_1155:
	s_waitcnt vmcnt(4) lgkmcnt(0)
	s_barrier
.LBB0_1159:
	ds_read_b128 v[52:55], v140
	ds_read_b128 v[190:193], v140 offset:512
	ds_read_b128 v[194:197], v140 offset:2048
	ds_read_b128 v[198:201], v140 offset:2560
	s_setprio 1
	s_waitcnt lgkmcnt(0)
	v_mfma_f32_32x32x16_bf16 v[68:83], v[52:55], v[136:139], v[36:51]
	v_add_f32_e32 v56, v100, v101
	ds_read_b128 v[202:205], v140 offset:4096
	ds_read_b64_tr_b16 v[172:173], v141 offset:49152
	ds_read_b64_tr_b16 v[174:175], v141 offset:49664
	v_add_f32_e32 v52, v102, v56
	v_add_f32_e32 v52, v103, v52
	v_add_f32_e32 v52, v104, v52
	v_add_f32_e32 v144, v105, v52
	v_cvt_pk_bf16_f32 v156, v100, v101
	v_cvt_pk_bf16_f32 v157, v102, v103
	v_exp_f32_e32 v92, v92
	v_exp_f32_e32 v93, v93
	v_exp_f32_e32 v94, v94
	v_exp_f32_e32 v95, v95
	v_mfma_f32_32x32x16_bf16 v[52:67], v[190:193], v[136:139], v[36:51]
	ds_read_b128 v[190:193], v140 offset:4608
	ds_read_b64_tr_b16 v[100:101], v141 offset:53248
	ds_read_b64_tr_b16 v[102:103], v141 offset:53760
	v_add_f32_e32 v144, v106, v144
	v_add_f32_e32 v144, v107, v144
	v_add_f32_e32 v144, v108, v144
	v_add_f32_e32 v144, v109, v144
	v_cvt_pk_bf16_f32 v158, v104, v105
	v_cvt_pk_bf16_f32 v159, v106, v107
	v_exp_f32_e32 v96, v96
	v_exp_f32_e32 v97, v97
	v_exp_f32_e32 v98, v98
	v_exp_f32_e32 v99, v99
	v_mfma_f32_32x32x16_bf16 v[68:83], v[194:197], v[132:135], v[68:83]
	ds_read_b128 v[194:197], v140 offset:6144
	ds_read_b64_tr_b16 v[104:105], v141 offset:50176
	ds_read_b64_tr_b16 v[106:107], v141 offset:50688
	v_add_f32_e32 v144, v110, v144
	v_add_f32_e32 v144, v111, v144
	v_add_f32_e32 v144, v112, v144
	v_add_f32_e32 v144, v113, v144
	v_cvt_pk_bf16_f32 v160, v108, v109
	v_cvt_pk_bf16_f32 v161, v110, v111
	v_mfma_f32_32x32x16_bf16 v[52:67], v[198:201], v[132:135], v[52:67]
	ds_read_b128 v[198:201], v140 offset:6656
	ds_read_b64_tr_b16 v[108:109], v141 offset:54272
	ds_read_b64_tr_b16 v[110:111], v141 offset:54784
	v_add_f32_e32 v144, v114, v144
	v_add_f32_e32 v144, v115, v144
	v_add_f32_e32 v144, v84, v144
	v_add_f32_e32 v144, v85, v144
	v_cvt_pk_bf16_f32 v162, v112, v113
	v_cvt_pk_bf16_f32 v163, v114, v115
	s_waitcnt lgkmcnt(0)
	v_mfma_f32_32x32x16_bf16 v[68:83], v[202:205], v[128:131], v[68:83]
	ds_read_b128 v[202:205], v140 offset:8192
	ds_read_b64_tr_b16 v[112:113], v141 offset:51200
	ds_read_b64_tr_b16 v[114:115], v141 offset:51712
	v_add_f32_e32 v144, v86, v144
	v_add_f32_e32 v144, v87, v144
	v_add_f32_e32 v144, v88, v144
	v_add_f32_e32 v144, v89, v144
	v_cvt_pk_bf16_f32 v164, v84, v85
	v_cvt_pk_bf16_f32 v165, v86, v87
	v_mfma_f32_32x32x16_bf16 v[52:67], v[190:193], v[128:131], v[52:67]
	ds_read_b128 v[190:193], v140 offset:8704
	ds_read_b64_tr_b16 v[84:85], v141 offset:55296
	ds_read_b64_tr_b16 v[86:87], v141 offset:55808
	v_add_f32_e32 v144, v90, v144
	v_add_f32_e32 v144, v91, v144
	v_add_f32_e32 v144, v92, v144
	v_add_f32_e32 v144, v93, v144
	v_cvt_pk_bf16_f32 v166, v88, v89
	v_cvt_pk_bf16_f32 v167, v90, v91
	v_mfma_f32_32x32x16_bf16 v[68:83], v[194:197], v[124:127], v[68:83]
	ds_read_b128 v[194:197], v140 offset:10240
	ds_read_b64_tr_b16 v[88:89], v141 offset:52224
	ds_read_b64_tr_b16 v[90:91], v141 offset:52736
	v_add_f32_e32 v144, v94, v144
	v_add_f32_e32 v144, v95, v144
	v_add_f32_e32 v144, v96, v144
	v_add_f32_e32 v144, v97, v144
	v_cvt_pk_bf16_f32 v168, v92, v93
	v_cvt_pk_bf16_f32 v169, v94, v95
	v_mfma_f32_32x32x16_bf16 v[52:67], v[198:201], v[124:127], v[52:67]
	ds_read_b128 v[198:201], v140 offset:10752
	ds_read_b64_tr_b16 v[92:93], v141 offset:56320
	ds_read_b64_tr_b16 v[94:95], v141 offset:56832
	v_add_f32_e32 v140, v98, v144
	v_add_f32_e32 v140, v99, v140
	v_cvt_pk_bf16_f32 v170, v96, v97
	v_cvt_pk_bf16_f32 v171, v98, v99
	s_waitcnt lgkmcnt(0)
	v_mfma_f32_32x32x16_bf16 v[68:83], v[202:205], v[120:123], v[68:83]
	s_add_i32 s8, s27, 3
	s_min_i32 s8, s8, s2
	s_lshl_b64 s[10:11], s[8:9], 17
	v_lshl_add_u64 v[202:203], v[176:177], 0, s[10:11]
	s_add_i32 s10, s26, s20
	s_mov_b32 m0, s10
	s_nop 0
	global_load_lds_dwordx4 v[202:203], off
	v_mfma_f32_32x32x16_bf16 v[52:67], v[190:193], v[120:123], v[52:67]
	s_and_b64 vcc, exec, s[38:39]
	s_cbranch_vccnz .Lmla_rope2
	s_lshl_b64 s[12:13], s[8:9], 18
	v_lshl_add_u64 v[202:203], v[180:181], 0, s[12:13]
	s_add_i32 m0, s10, 0x2000
	s_nop 0
	global_load_lds_dwordx4 v[202:203], off

; __device__ __forceinline__ void mla_unit(int b, int h, int qb, const bf16_t* __restrict__ Q, const bf16_t* __restrict__ KV, const bf16_t* __restrict__ PROJ, bf16_t* OCAT, float* SSQO, ldsp shm) {
;     ...
;     int t = 1;
;     for (; t + 1 < NT; t += 2) { STEP(pB0, pB1, pA0, pA1, t); STEP(pA0, pA1, pB0, pB1, t + 1); }
.LBB0_1163:
	v_mfma_f32_32x32x16_bf16 v[4:19], v[156:159], v[172:175], v[4:19]
	v_exp_f32_e32 v68, v68
	v_exp_f32_e32 v69, v69
	v_exp_f32_e32 v70, v70
	v_exp_f32_e32 v71, v71
	v_mfma_f32_32x32x16_bf16 v[20:35], v[156:159], v[100:103], v[20:35]
	v_exp_f32_e32 v72, v72
	v_exp_f32_e32 v73, v73
	v_exp_f32_e32 v74, v74
	v_exp_f32_e32 v75, v75
	s_add_i32 s12, s16, -1
	s_and_b32 s12, s12, 3
	s_mulk_i32 s12, 0x3000
	v_add_u32_e32 v156, s12, v188
	s_add_i32 s12, s14, 0x4000
	s_and_b32 s12, s12, 0x6000
	v_add_u32_e32 v157, s12, v186
	v_mfma_f32_32x32x16_bf16 v[4:19], v[160:163], v[104:107], v[4:19]
	v_exp_f32_e32 v76, v76
	v_exp_f32_e32 v77, v77
	v_exp_f32_e32 v78, v78
	v_exp_f32_e32 v79, v79
	v_mfma_f32_32x32x16_bf16 v[20:35], v[160:163], v[108:111], v[20:35]
	v_exp_f32_e32 v80, v80
	v_exp_f32_e32 v81, v81
	v_exp_f32_e32 v82, v82
	v_exp_f32_e32 v83, v83
	v_mfma_f32_32x32x16_bf16 v[4:19], v[164:167], v[112:115], v[4:19]
	v_exp_f32_e32 v52, v52
	v_exp_f32_e32 v53, v53
	v_exp_f32_e32 v54, v54
	v_exp_f32_e32 v55, v55
	v_mfma_f32_32x32x16_bf16 v[20:35], v[164:167], v[84:87], v[20:35]
	v_exp_f32_e32 v56, v56
	v_exp_f32_e32 v57, v57
	v_exp_f32_e32 v58, v58
	v_exp_f32_e32 v59, v59
	v_mfma_f32_32x32x16_bf16 v[4:19], v[168:171], v[88:91], v[4:19]
	v_mfma_f32_32x32x16_bf16 v[20:35], v[168:171], v[92:95], v[20:35]
	s_and_b64 vcc, exec, s[10:11]
	s_cbranch_vccnz .Lmla_resc2
.LBB0_1165:
	s_addk_i32 s14, 0x4000
	s_add_i32 s12, s16, -1
	s_cmp_lt_u32 s12, s2
	s_cbranch_scc0 .LBB0_1175
	s_mov_b32 s27, s16
	s_branch .LBB0_1146
.Lmla_resc2:
	s_waitcnt lgkmcnt(0)
	v_add_u32_e32 v96, s51, v2
	ds_read_b128 v[84:87], v96 offset:96
	ds_read_b128 v[88:91], v96 offset:64
	ds_read_b128 v[92:95], v96 offset:32
	ds_read_b128 v[96:99], v96
	s_waitcnt lgkmcnt(0)
	v_pk_mul_f32 v[16:17], v[16:17], v[84:85]
	v_pk_mul_f32 v[12:13], v[12:13], v[88:89]
	v_pk_mul_f32 v[8:9], v[8:9], v[92:93]
	v_pk_mul_f32 v[18:19], v[18:19], v[86:87]
	v_pk_mul_f32 v[14:15], v[14:15], v[90:91]
	v_pk_mul_f32 v[10:11], v[10:11], v[94:95]
	v_pk_mul_f32 v[6:7], v[6:7], v[98:99]
	v_pk_mul_f32 v[4:5], v[4:5], v[96:97]
	v_pk_mul_f32 v[32:33], v[32:33], v[84:85]
	v_pk_mul_f32 v[28:29], v[28:29], v[88:89]
	v_pk_mul_f32 v[24:25], v[24:25], v[92:93]
	v_pk_mul_f32 v[34:35], v[34:35], v[86:87]
	v_pk_mul_f32 v[30:31], v[30:31], v[90:91]
	v_pk_mul_f32 v[26:27], v[26:27], v[94:95]
	v_pk_mul_f32 v[22:23], v[22:23], v[98:99]
	v_pk_mul_f32 v[20:21], v[20:21], v[96:97]
	s_branch .LBB0_1165
.Lmla_resc1:
	s_waitcnt lgkmcnt(0)
	v_add_u32_e32 v64, s51, v2
	ds_read_b128 v[52:55], v64 offset:96
	ds_read_b128 v[56:59], v64 offset:64
	ds_read_b128 v[60:63], v64 offset:32
	ds_read_b128 v[64:67], v64
	s_waitcnt lgkmcnt(0)
	v_pk_mul_f32 v[16:17], v[16:17], v[52:53]
	v_pk_mul_f32 v[12:13], v[12:13], v[56:57]
	v_pk_mul_f32 v[8:9], v[8:9], v[60:61]
	v_pk_mul_f32 v[18:19], v[18:19], v[54:55]
	v_pk_mul_f32 v[14:15], v[14:15], v[58:59]
	v_pk_mul_f32 v[10:11], v[10:11], v[62:63]
	v_pk_mul_f32 v[6:7], v[6:7], v[66:67]
	v_pk_mul_f32 v[4:5], v[4:5], v[64:65]
	v_pk_mul_f32 v[32:33], v[32:33], v[52:53]
	v_pk_mul_f32 v[28:29], v[28:29], v[56:57]
	v_pk_mul_f32 v[24:25], v[24:25], v[60:61]
	v_pk_mul_f32 v[34:35], v[34:35], v[54:55]
	v_pk_mul_f32 v[30:31], v[30:31], v[58:59]
	v_pk_mul_f32 v[26:27], v[26:27], v[62:63]
	v_pk_mul_f32 v[22:23], v[22:23], v[66:67]
	v_pk_mul_f32 v[20:21], v[20:21], v[64:65]
	s_branch .LBB0_1155

; __device__ __forceinline__ void mla_unit(int b, int h, int qb, const bf16_t* __restrict__ Q, const bf16_t* __restrict__ KV, const bf16_t* __restrict__ PROJ, bf16_t* OCAT, float* SSQO, ldsp shm) {
;     ...
;     for (; t + 1 < NT; t += 2) { STEP(pB0, pB1, pA0, pA1, t); STEP(pA0, pA1, pB0, pB1, t + 1); }
;     STEP(pB0, pB1, pA0, pA1, t);
.LBB0_1172:
	v_max_f32_e32 v36, v96, v96
	v_max_f32_e32 v96, 0, v36
	v_exp_f32_e64 v97, -v96
	v_add_f32_e32 v187, v187, v96
	v_xor_b32_e32 v36, 0x80000000, v187
	v_mov_b32_e32 v37, v36
	v_mov_b32_e32 v38, v36
	v_mov_b32_e32 v39, v36
	v_mov_b32_e32 v40, v36
	v_mov_b32_e32 v41, v36
	v_mov_b32_e32 v42, v36
	v_mov_b32_e32 v43, v36
	v_mov_b32_e32 v44, v36
	v_mov_b32_e32 v45, v36
	v_mov_b32_e32 v46, v36
	v_mov_b32_e32 v47, v36
	v_mov_b32_e32 v48, v36
	v_mov_b32_e32 v49, v36
	v_mov_b32_e32 v50, v36
	v_mov_b32_e32 v51, v36
	s_and_saveexec_b64 s[12:13], s[36:37]
	ds_write_b32 v185, v97
	s_or_b64 exec, exec, s[12:13]
	v_sub_f32_e32 v83, v83, v96
	v_sub_f32_e32 v82, v82, v96
	v_sub_f32_e32 v81, v81, v96
	v_sub_f32_e32 v80, v80, v96
	v_sub_f32_e32 v79, v79, v96
	v_sub_f32_e32 v78, v78, v96
	v_sub_f32_e32 v77, v77, v96
	v_sub_f32_e32 v76, v76, v96
	v_sub_f32_e32 v75, v75, v96
	v_sub_f32_e32 v74, v74, v96
	v_sub_f32_e32 v73, v73, v96
	v_sub_f32_e32 v72, v72, v96
	v_sub_f32_e32 v71, v71, v96
	v_sub_f32_e32 v70, v70, v96
	v_sub_f32_e32 v69, v69, v96
	v_sub_f32_e32 v68, v68, v96
	v_sub_f32_e32 v67, v67, v96
	v_sub_f32_e32 v66, v66, v96
	v_sub_f32_e32 v65, v65, v96
	v_sub_f32_e32 v64, v64, v96
	v_sub_f32_e32 v63, v63, v96
	v_sub_f32_e32 v62, v62, v96
	v_sub_f32_e32 v61, v61, v96
	v_sub_f32_e32 v60, v60, v96
	v_sub_f32_e32 v59, v59, v96
	v_sub_f32_e32 v58, v58, v96
	v_sub_f32_e32 v57, v57, v96
	v_sub_f32_e32 v56, v56, v96
	v_sub_f32_e32 v55, v55, v96
	v_sub_f32_e32 v54, v54, v96
	v_sub_f32_e32 v53, v53, v96
	v_sub_f32_e32 v52, v52, v96
	v_mul_f32_e32 v189, v189, v97
	s_branch .LBB0_1163
.LBB0_1175:
	s_waitcnt vmcnt(4) lgkmcnt(0)
	s_barrier
.LBB0_1179:
	ds_read_b128 v[100:103], v156
	ds_read_b128 v[104:107], v156 offset:512
	ds_read_b128 v[108:111], v156 offset:2048
	ds_read_b128 v[112:115], v156 offset:2560
	s_add_i32 s3, s17, 0
	s_lshl_b32 s8, s2, 17
	s_add_i32 s3, s3, s34
	v_lshl_add_u64 v[84:85], v[176:177], 0, s[8:9]
	s_mov_b32 m0, s3
	s_and_b64 vcc, exec, s[38:39]
	global_load_lds_dwordx4 v[84:85], off
	s_cbranch_vccnz .LBB0_1181
	s_lshl_b32 s10, s2, 18
	s_mov_b32 s11, s9
	v_lshl_add_u64 v[84:85], v[180:181], 0, s[10:11]
	s_add_i32 m0, s3, 0x2000
	s_nop 0
	global_load_lds_dwordx4 v[84:85], off
